# conversion-first loop: bf16 transpose image rows skewed by 8 B per 16 rows so the 64-bit LDS writes are bank-conflict free (was 4-way)
# baseline (speedup 1.0000x reference)
; __device__ __forceinline__ void conv_queue(const P& p, LAS unsigned char* lds, int* ctr, int max_tiles) {
;     ...
;         CQ_PUT(0, 0); CQ_PUT(1, 1);
.LBB0_826:
	s_andn2_b64 vcc, exec, s[6:7]
	v_add_u32_e32 v84, 0x4000, v83
	v_bfe_u32 v244, v0, 2, 4
	v_lshl_add_u32 v84, v244, 3, v84
	s_cbranch_vccnz .LBB0_828
	s_waitcnt vmcnt(14)
	v_cvt_pk_bf16_f32 v74, v20, v24
	s_waitcnt vmcnt(12)
	v_cvt_pk_bf16_f32 v75, v28, v32
	v_cvt_pk_bf16_f32 v86, v21, v25
	v_cvt_pk_bf16_f32 v87, v29, v33
	ds_write2_b64 v84, v[74:75], v[86:87] offset1:33
	v_cvt_pk_bf16_f32 v74, v22, v26
	v_cvt_pk_bf16_f32 v75, v30, v34
	v_cvt_pk_bf16_f32 v86, v23, v27
	v_cvt_pk_bf16_f32 v87, v31, v35
	ds_write2_b64 v84, v[74:75], v[86:87] offset0:66 offset1:99

; #define LAS __attribute__((address_space(3)))
; __device__ __forceinline__ void fp6_block_bf16(const u32x16& w, u32x4& out_lo, u32x4& out_hi) {
;     typedef unsigned short u16x2_t __attribute__((ext_vector_type(2))); u16x2_t mx = {0, 0};
; #pragma unroll
;     for (int i = 0; i < 16; ++i) mx = __builtin_elementwise_max(mx, __builtin_bit_cast(u16x2_t, w[i] & 0x7fff7fffu));
;     const unsigned am = mx[0] > mx[1] ? mx[0] : mx[1];
;     int sb = (int)((am + 15u) >> 7) - 2; sb = sb < 7 ? 7 : sb;
;     const u32x6 c = __builtin_amdgcn_cvt_scalef32_pk32_fp6_bf16(__builtin_bit_cast(bf16x32_t, w), __uint_as_float((unsigned)sb << 23));
;     out_lo.x = c[0]; out_lo.y = c[1]; out_lo.z = c[2]; out_lo.w = c[3];
;     out_hi.x = c[4]; out_hi.y = c[5]; out_hi.z = (unsigned)sb; out_hi.w = 0u;
; }
; __device__ __forceinline__ void conv_queue(const P& p, LAS unsigned char* lds, int* ctr, int max_tiles) {
;     ...
;           if (cur_w1) {
;               unsigned char* Bt = p.ws + WS_W1_T + (size_t)e_ * 4096 * 2048;
; #pragma unroll 1
;               for (int ps = 0; ps < 2; ++ps) { const int id = tid + 512 * ps, n = id >> 2, q = id & 3; const LAS u32x2* tp_ = (const LAS u32x2*)(Tb + n * 264 + q * 64);
;                   u32x16 wv;
; #pragma unroll
;                   for (int i = 0; i < 8; ++i) { const u32x2 w = tp_[i]; wv[2 * i] = w.x; wv[2 * i + 1] = w.y; }
;                   u32x4 lo, hi; fp6_block_bf16(wv, lo, hi);
;                   unsigned char* dst = Bt + (size_t)DmW1{}(n0 + n) * 2048 + k0 + 16 * q;
;                   __builtin_nontemporal_store(lo, (u32x4*)dst); __builtin_nontemporal_store(hi, (u32x4*)(dst + 64)); }
.LBB0_850:
	v_cndmask_b32_e64 v2, 0, 1, s[6:7]
	v_add_u32_e32 v3, s11, v0
	v_cmp_ne_u32_e32 vcc, 1, v2
	v_lshrrev_b32_e32 v2, 2, v3
	v_bfe_u32 v18, v3, 3, 7
	v_mad_u32_u24 v3, v2, s2, v77
	v_lshrrev_b32_e32 v244, 4, v2
	v_lshl_add_u32 v3, v244, 3, v3
	v_add_u32_e32 v2, s8, v2
	v_lshlrev_b32_e32 v56, 7, v2
	v_add_u32_e32 v4, 0x4000, v3
	v_add_u32_e32 v6, 0x4010, v3
	v_add_u32_e32 v10, 0x4020, v3
	v_add_u32_e32 v14, 0x4030, v3
	v_and_b32_e32 v54, 0x1f00, v2
	v_and_b32_e32 v56, 0x80, v56
	ds_read2_b64 v[2:5], v4 offset1:1
	ds_read2_b64 v[6:9], v6 offset1:1
	ds_read2_b64 v[10:13], v10 offset1:1
	ds_read2_b64 v[14:17], v14 offset1:1
	v_or3_b32 v18, v54, v56, v18
	v_mov_b32_e32 v55, v19
	v_lshlrev_b32_e32 v54, 11, v18
	v_lshl_add_u64 v[60:61], v[52:53], 0, v[54:55]
	s_waitcnt lgkmcnt(3)
	v_and_b32_e32 v18, 0x7fff7fff, v2
	v_and_b32_e32 v54, 0x7fff7fff, v3
	v_and_b32_e32 v55, 0x7fff7fff, v4
	v_pk_max_u16 v18, v18, v54
	v_and_b32_e32 v56, 0x7fff7fff, v5
	v_pk_max_u16 v18, v18, v55
	s_waitcnt lgkmcnt(2)
	v_and_b32_e32 v57, 0x7fff7fff, v6
	v_pk_max_u16 v18, v18, v56
	v_and_b32_e32 v58, 0x7fff7fff, v7
	v_pk_max_u16 v18, v18, v57
	v_and_b32_e32 v59, 0x7fff7fff, v8
	v_pk_max_u16 v18, v18, v58
	v_and_b32_e32 v62, 0x7fff7fff, v9
	v_pk_max_u16 v18, v18, v59
	s_waitcnt lgkmcnt(1)
	v_and_b32_e32 v63, 0x7fff7fff, v10
	v_pk_max_u16 v18, v18, v62
	v_and_b32_e32 v64, 0x7fff7fff, v11
	v_pk_max_u16 v18, v18, v63
	v_and_b32_e32 v65, 0x7fff7fff, v12
	v_pk_max_u16 v18, v18, v64
	v_and_b32_e32 v66, 0x7fff7fff, v13
	v_pk_max_u16 v18, v18, v65
	s_waitcnt lgkmcnt(0)
	v_and_b32_e32 v67, 0x7fff7fff, v14
	v_pk_max_u16 v18, v18, v66
	v_and_b32_e32 v73, 0x7fff7fff, v15
	v_pk_max_u16 v18, v18, v67
	v_and_b32_e32 v84, 0x7fff7fff, v16
	v_pk_max_u16 v18, v18, v73
	v_and_b32_e32 v85, 0x7fff7fff, v17
	v_pk_max_u16 v18, v18, v84
	s_movk_i32 s11, 0x200
	v_pk_max_u16 v18, v18, v85
	s_mov_b64 s[6:7], 0
	v_max_u16_sdwa v18, v18, v18 dst_sel:DWORD dst_unused:UNUSED_PAD src0_sel:DWORD src1_sel:WORD_1
	v_add_u32_e32 v18, 15, v18
	v_lshrrev_b32_e32 v18, 7, v18
	v_max_u32_e32 v18, 9, v18
	v_add_u32_e32 v18, -2, v18
	v_lshlrev_b32_e32 v62, 23, v18
	s_and_b64 vcc, exec, vcc
	v_cvt_scalef32_pk32_fp6_bf16 v[54:59], v[2:17], v62
	v_mov_b32_e32 v16, v58
	v_mov_b32_e32 v17, v59
	global_store_dwordx4 v[60:61], v[54:57], off nt
	global_store_dwordx4 v[60:61], v[16:19], off offset:64 nt
	s_cbranch_vccz .LBB0_850
